# P1 column-tile order permuted so every CU gets one unit of each epilogue kind (balances silu/gelu epilogue cost across XCDs) + P2 LDS read hoists
# speedup vs baseline: 1.0114x; 1.0114x over previous
.LBB0_100:
	s_or_b64 exec, exec, s[0:1]
	s_mov_b64 s[0:1], s[82:83]
	v_mov_b32_e32 v10, v0
	s_cmpk_lt_i32 s80, 0x600
	s_waitcnt lgkmcnt(0)
	s_barrier
	v_mbcnt_lo_u32_b32 v1, -1, 0
	v_mbcnt_hi_u32_b32 v1, -1, v1
	s_cselect_b64 s[2:3], -1, 0
	s_cmpk_gt_i32 s80, 0x5ff
	v_readfirstlane_b32 s4, v10
	s_cbranch_scc1 .LBB0_102
	s_ashr_i32 s5, s80, 31
	s_lshr_b32 s5, s5, 29
	s_add_i32 s5, s80, s5
	s_ashr_i32 s6, s5, 3
	s_and_b32 s5, s5, -8
	s_sub_i32 s5, s80, s5
	s_cmp_lt_i32 s5, 0
	s_movk_i32 s7, 0xc1
	s_cselect_b32 s7, s7, 0xc0
	s_mul_i32 s5, s5, s7
	s_add_i32 s5, s5, s6
	s_mul_hi_i32 s6, s5, 0x2aaaaaab
	s_lshr_b32 s7, s6, 31
	s_ashr_i32 s6, s6, 6
	s_add_i32 s6, s6, s7
	s_lshl_b32 s7, s6, 3
	s_mulk_i32 s6, 0x180
	s_sub_i32 s5, s5, s6
	s_sext_i32_i16 s6, s5
	s_bfe_u32 s6, s6, 0x3001c
	s_add_i32 s6, s5, s6
	s_sext_i32_i16 s8, s6
	s_and_b32 s6, s6, 0xfff8
	s_sub_i32 s5, s5, s6
	s_sext_i32_i16 s5, s5
	s_add_i32 s24, s7, s5
	s_ashr_i32 s6, s8, 3
	s_cmp_ge_u32 s6, 24
	s_cselect_b32 s98, 1, 0
	s_cselect_b32 s99, 24, 0
	s_sub_i32 s6, s6, s99
	s_lshl_b32 s6, s6, 1
	s_or_b32 s6, s6, s98

.LBB0_108:
	s_add_i32 s50, s22, 1
	s_mul_i32 s3, s50, s45
	s_mul_hi_u32 s4, s50, s81
	s_add_i32 s4, s4, s3
	s_mul_i32 s3, s50, s81
	s_add_u32 s16, s3, s80
	s_addc_u32 s17, s4, s46
	v_cmp_gt_i64_e32 vcc, s[16:17], v[164:165]
	v_cmp_lt_i64_e64 s[4:5], s[16:17], v[162:163]
	s_cbranch_vccnz .LBB0_110
	s_ashr_i32 s2, s16, 31
	s_lshr_b32 s2, s2, 29
	s_add_i32 s2, s16, s2
	s_ashr_i32 s3, s2, 3
	s_and_b32 s2, s2, -8
	s_sub_i32 s2, s16, s2
	s_cmp_lt_i32 s2, 0
	s_cselect_b32 s7, s47, 0xc0
	s_mul_i32 s2, s2, s7
	s_add_i32 s2, s2, s3
	s_mul_hi_i32 s3, s2, 0x2aaaaaab
	s_lshr_b32 s7, s3, 31
	s_ashr_i32 s3, s3, 6
	s_add_i32 s3, s3, s7
	s_lshl_b32 s7, s3, 3
	s_sub_i32 s14, 32, s7
	s_min_i32 s14, s14, 8
	s_abs_i32 s15, s14
	v_cvt_f32_u32_e32 v2, s15
	s_sub_i32 s17, 0, s15
	s_mulk_i32 s3, 0x180
	s_sub_i32 s3, s2, s3
	v_rcp_iflag_f32_e32 v2, v2
	s_abs_i32 s2, s3
	s_xor_b32 s16, s3, s14
	s_ashr_i32 s16, s16, 31
	v_mul_f32_e32 v2, 0x4f7ffffe, v2
	v_cvt_u32_f32_e32 v2, v2
	s_nop 0
	v_readfirstlane_b32 s18, v2
	s_mul_i32 s17, s17, s18
	s_mul_hi_u32 s17, s18, s17
	s_add_i32 s18, s18, s17
	s_mul_hi_u32 s17, s2, s18
	s_mul_i32 s18, s17, s15
	s_sub_i32 s2, s2, s18
	s_add_i32 s19, s17, 1
	s_sub_i32 s18, s2, s15
	s_cmp_ge_u32 s2, s15
	s_cselect_b32 s17, s19, s17
	s_cselect_b32 s2, s18, s2
	s_add_i32 s18, s17, 1
	s_cmp_ge_u32 s2, s15
	s_cselect_b32 s2, s18, s17
	s_xor_b32 s2, s2, s16
	s_sub_i32 s2, s2, s16
	s_mul_i32 s14, s2, s14
	s_sub_i32 s3, s3, s14
	s_add_i32 s14, s7, s3
	s_cmp_ge_u32 s2, 24
	s_cselect_b32 s98, 1, 0
	s_cselect_b32 s99, 24, 0
	s_sub_i32 s2, s2, s99
	s_lshl_b32 s2, s2, 1
	s_or_b32 s2, s2, s98
